# stream: per-block rotation of wave-to-row assignment (row = blk*128+i*16+((w+blk)&15)); prep rewrite kept
# speedup vs baseline: 1.0151x; 1.0151x over previous
.LBB1_2:
	s_or_b64 exec, exec, s[0:1]
	s_lshr_b32 s8, s3, 6
	s_add_i32 s8, s8, s2
	s_and_b32 s8, s8, 15
	s_lshl_b32 s0, s2, 7
	v_and_b32_e32 v24, 63, v0
	s_add_i32 s9, s8, s0
	s_waitcnt lgkmcnt(0)
	s_and_b32 s1, s5, 0xffff
	s_mov_b32 s3, 0x20000
	s_brev_b32 s2, 16
	s_mov_b32 s0, s4
	v_lshlrev_b32_e32 v25, 4, v24
	s_lshl_b32 s4, s9, 12
	buffer_load_dwordx4 v[26:29], v25, s[0:3], s4 offen offset:1024 nt
	buffer_load_dwordx4 v[30:33], v25, s[0:3], s4 offen nt
	buffer_load_dwordx4 v[34:37], v25, s[0:3], s4 offen offset:2048 nt
	s_add_i32 s5, s4, 0x10000
	buffer_load_dwordx4 v[38:41], v25, s[0:3], s5 offen offset:1024 nt
	buffer_load_dwordx4 v[42:45], v25, s[0:3], s5 offen nt
	buffer_load_dwordx4 v[16:19], v25, s[0:3], s4 offen offset:3072 nt
	s_add_i32 s10, s4, 0x20000
	buffer_load_dwordx4 v[46:49], v25, s[0:3], s5 offen offset:2048 nt
	buffer_load_dwordx4 v[20:23], v25, s[0:3], s5 offen offset:3072 nt
	s_barrier
	buffer_load_dwordx4 v[50:53], v25, s[0:3], s10 offen offset:1024 nt
	buffer_load_dwordx4 v[54:57], v25, s[0:3], s10 offen nt
	ds_read_b128 v[4:7], v25 offset:1024
	ds_read_b128 v[0:3], v25
	ds_read_b128 v[12:15], v25 offset:2048
	ds_read_b128 v[8:11], v25 offset:3072
	s_add_i32 s5, s4, 0x30000
	v_cmp_gt_u32_e32 vcc, 8, v24
	s_waitcnt vmcnt(9) lgkmcnt(3)
	v_pk_mul_f32 v[28:29], v[6:7], v[28:29]
	v_pk_mul_f32 v[26:27], v[4:5], v[26:27]
	s_waitcnt vmcnt(8) lgkmcnt(2)
	v_pk_fma_f32 v[32:33], v[2:3], v[32:33], v[28:29]
	v_pk_fma_f32 v[30:31], v[0:1], v[30:31], v[26:27]
	buffer_load_dwordx4 v[26:29], v25, s[0:3], s5 offen offset:1024 nt
	s_waitcnt vmcnt(8) lgkmcnt(1)
	v_pk_fma_f32 v[58:59], v[14:15], v[36:37], v[32:33]
	v_pk_fma_f32 v[60:61], v[12:13], v[34:35], v[30:31]
	buffer_load_dwordx4 v[30:33], v25, s[0:3], s5 offen nt
	s_waitcnt vmcnt(8)
	v_pk_mul_f32 v[34:35], v[6:7], v[40:41]
	v_pk_mul_f32 v[36:37], v[4:5], v[38:39]
	s_waitcnt vmcnt(7)
	v_pk_fma_f32 v[44:45], v[2:3], v[44:45], v[34:35]
	v_pk_fma_f32 v[42:43], v[0:1], v[42:43], v[36:37]
	buffer_load_dwordx4 v[34:37], v25, s[0:3], s10 offen offset:2048 nt
	s_waitcnt vmcnt(4)
	v_pk_mul_f32 v[38:39], v[6:7], v[52:53]
	v_pk_mul_f32 v[40:41], v[4:5], v[50:51]
	s_waitcnt vmcnt(3)
	v_pk_fma_f32 v[50:51], v[2:3], v[56:57], v[38:39]
	v_pk_fma_f32 v[52:53], v[0:1], v[54:55], v[40:41]
	buffer_load_dwordx4 v[38:41], v25, s[0:3], s10 offen offset:3072 nt
	v_pk_fma_f32 v[48:49], v[14:15], v[48:49], v[44:45]
	v_pk_fma_f32 v[46:47], v[12:13], v[46:47], v[42:43]
	s_waitcnt lgkmcnt(0)
	v_pk_fma_f32 v[18:19], v[10:11], v[18:19], v[58:59]
	v_pk_fma_f32 v[16:17], v[8:9], v[16:17], v[60:61]
	v_add_f32_e32 v61, v18, v19
	v_add_f32_e32 v60, v16, v17
	v_pk_fma_f32 v[16:17], v[10:11], v[22:23], v[48:49]
	v_pk_fma_f32 v[18:19], v[8:9], v[20:21], v[46:47]
	v_add_f32_e32 v16, v16, v17
	v_add_f32_e32 v18, v18, v19
	v_add_f32_e32 v60, v60, v61
	v_add_f32_e32 v16, v18, v16
	s_add_i32 s10, s4, 0x50000
	s_waitcnt vmcnt(3)
	v_pk_mul_f32 v[28:29], v[6:7], v[28:29]
	v_pk_mul_f32 v[26:27], v[4:5], v[26:27]
	v_add_f32_dpp v16, v16, v16 quad_perm:[1,0,3,2] row_mask:0xf bank_mask:0xf bound_ctrl:1
	s_waitcnt vmcnt(2)
	v_pk_fma_f32 v[54:55], v[2:3], v[32:33], v[28:29]
	v_pk_fma_f32 v[56:57], v[0:1], v[30:31], v[26:27]
	buffer_load_dwordx4 v[26:29], v25, s[0:3], s5 offen offset:2048 nt
	buffer_load_dwordx4 v[30:33], v25, s[0:3], s5 offen offset:3072 nt
	s_add_i32 s5, s4, 0x40000
	buffer_load_dwordx4 v[42:45], v25, s[0:3], s5 offen offset:1024 nt
	s_waitcnt vmcnt(4)
	v_pk_fma_f32 v[50:51], v[14:15], v[36:37], v[50:51]
	v_pk_fma_f32 v[52:53], v[12:13], v[34:35], v[52:53]
	buffer_load_dwordx4 v[34:37], v25, s[0:3], s5 offen nt
	v_add_f32_dpp v16, v16, v16 quad_perm:[2,3,0,1] row_mask:0xf bank_mask:0xf bound_ctrl:1
	s_waitcnt vmcnt(4)
	v_pk_fma_f32 v[58:59], v[10:11], v[40:41], v[50:51]
	v_pk_fma_f32 v[38:39], v[8:9], v[38:39], v[52:53]
	v_add_f32_e32 v19, v58, v59
	v_add_f32_e32 v17, v38, v39
	v_add_f32_dpp v58, v60, v60 quad_perm:[1,0,3,2] row_mask:0xf bank_mask:0xf bound_ctrl:1
	v_add_f32_e32 v18, v17, v19
	v_add_f32_dpp v16, v16, v16 row_ror:4 row_mask:0xf bank_mask:0xf bound_ctrl:1
	v_add_f32_dpp v17, v58, v58 quad_perm:[2,3,0,1] row_mask:0xf bank_mask:0xf bound_ctrl:1
	buffer_load_dwordx4 v[20:23], v25, s[0:3], s5 offen offset:2048 nt
	buffer_load_dwordx4 v[46:49], v25, s[0:3], s5 offen offset:3072 nt
	v_add_f32_dpp v17, v17, v17 row_ror:4 row_mask:0xf bank_mask:0xf bound_ctrl:1
	v_add_f32_dpp v58, v16, v16 row_ror:8 row_mask:0xf bank_mask:0xf bound_ctrl:1
	buffer_load_dwordx4 v[38:41], v25, s[0:3], s10 offen nt
	buffer_load_dwordx4 v[50:53], v25, s[0:3], s10 offen offset:1024 nt
	v_add_f32_dpp v17, v17, v17 row_ror:8 row_mask:0xf bank_mask:0xf bound_ctrl:1
	v_mov_b32_e32 v19, v17
	v_mov_b32_e32 v59, v58
	s_nop 0
	v_permlane16_swap_b32_e32 v17, v19
	v_permlane16_swap_b32_e32 v58, v59
	v_add_f32_e32 v16, v17, v19
	v_add_f32_e32 v17, v58, v59
	s_add_i32 s5, s4, 0x60000
	s_add_i32 s4, s4, 0x70000
	v_add_f32_dpp v18, v18, v18 quad_perm:[1,0,3,2] row_mask:0xf bank_mask:0xf bound_ctrl:1
	s_waitcnt vmcnt(7)
	v_pk_fma_f32 v[28:29], v[14:15], v[28:29], v[54:55]
	v_pk_fma_f32 v[54:55], v[12:13], v[26:27], v[56:57]
	s_waitcnt vmcnt(6)
	v_pk_fma_f32 v[58:59], v[10:11], v[32:33], v[28:29]
	buffer_load_dwordx4 v[26:29], v25, s[0:3], s10 offen offset:2048 nt
	v_pk_fma_f32 v[54:55], v[8:9], v[30:31], v[54:55]
	buffer_load_dwordx4 v[30:33], v25, s[0:3], s10 offen offset:3072 nt
	v_add_f32_e32 v66, v54, v55
	s_waitcnt vmcnt(7)
	v_pk_mul_f32 v[54:55], v[6:7], v[44:45]
	v_pk_mul_f32 v[56:57], v[4:5], v[42:43]
	buffer_load_dwordx4 v[42:45], v25, s[0:3], s5 offen offset:1024 nt
	s_waitcnt vmcnt(7)
	v_pk_fma_f32 v[54:55], v[2:3], v[36:37], v[54:55]
	v_pk_fma_f32 v[56:57], v[0:1], v[34:35], v[56:57]
	buffer_load_dwordx4 v[34:37], v25, s[0:3], s5 offen nt
	v_add_f32_dpp v18, v18, v18 quad_perm:[2,3,0,1] row_mask:0xf bank_mask:0xf bound_ctrl:1
	s_waitcnt vmcnt(7)
	v_pk_fma_f32 v[22:23], v[14:15], v[22:23], v[54:55]
	v_pk_fma_f32 v[20:21], v[12:13], v[20:21], v[56:57]
	s_waitcnt vmcnt(6)
	v_pk_fma_f32 v[60:61], v[10:11], v[48:49], v[22:23]
	v_pk_fma_f32 v[22:23], v[8:9], v[46:47], v[20:21]
	s_waitcnt vmcnt(4)
	v_pk_mul_f32 v[54:55], v[4:5], v[50:51]
	v_pk_mul_f32 v[20:21], v[6:7], v[52:53]
	v_pk_fma_f32 v[38:39], v[0:1], v[38:39], v[54:55]
	buffer_load_dwordx4 v[46:49], v25, s[0:3], s5 offen offset:2048 nt
	buffer_load_dwordx4 v[50:53], v25, s[0:3], s5 offen offset:3072 nt
	v_pk_fma_f32 v[20:21], v[2:3], v[40:41], v[20:21]
	v_add_f32_e32 v23, v22, v23
	v_add_f32_dpp v18, v18, v18 row_ror:4 row_mask:0xf bank_mask:0xf bound_ctrl:1
	s_waitcnt vmcnt(5)
	v_pk_fma_f32 v[26:27], v[12:13], v[26:27], v[38:39]
	buffer_load_dwordx4 v[38:41], v25, s[0:3], s4 offen nt
	buffer_load_dwordx4 v[54:57], v25, s[0:3], s4 offen offset:1024 nt
	v_pk_fma_f32 v[20:21], v[14:15], v[28:29], v[20:21]
	s_waitcnt vmcnt(6)
	v_pk_fma_f32 v[30:31], v[8:9], v[30:31], v[26:27]
	v_pk_fma_f32 v[62:63], v[10:11], v[32:33], v[20:21]
	v_add_f32_dpp v18, v18, v18 row_ror:8 row_mask:0xf bank_mask:0xf bound_ctrl:1
	s_waitcnt vmcnt(5)
	v_pk_mul_f32 v[20:21], v[6:7], v[44:45]
	v_pk_mul_f32 v[26:27], v[4:5], v[42:43]
	buffer_load_dwordx4 v[42:45], v25, s[0:3], s4 offen offset:2048 nt
	s_waitcnt vmcnt(5)
	v_pk_fma_f32 v[64:65], v[0:1], v[34:35], v[26:27]
	buffer_load_dwordx4 v[32:35], v25, s[0:3], s4 offen offset:3072 nt
	v_add_f32_e32 v27, v60, v61
	v_add_f32_e32 v23, v23, v27
	v_pk_fma_f32 v[36:37], v[2:3], v[36:37], v[20:21]
	v_add_f32_e32 v20, v58, v59
	v_add_f32_dpp v23, v23, v23 quad_perm:[1,0,3,2] row_mask:0xf bank_mask:0xf bound_ctrl:1
	v_add_f32_e32 v20, v66, v20
	v_mov_b32_e32 v19, v18
	v_add_f32_dpp v23, v23, v23 quad_perm:[2,3,0,1] row_mask:0xf bank_mask:0xf bound_ctrl:1
	v_add_f32_dpp v20, v20, v20 quad_perm:[1,0,3,2] row_mask:0xf bank_mask:0xf bound_ctrl:1
	v_permlane16_swap_b32_e32 v18, v19
	v_add_f32_dpp v23, v23, v23 row_ror:4 row_mask:0xf bank_mask:0xf bound_ctrl:1
	v_add_f32_dpp v20, v20, v20 quad_perm:[2,3,0,1] row_mask:0xf bank_mask:0xf bound_ctrl:1
	v_add_f32_e32 v18, v18, v19
	v_add_f32_dpp v23, v23, v23 row_ror:8 row_mask:0xf bank_mask:0xf bound_ctrl:1
	v_mov_b32_e32 v27, v23
	s_nop 1
	v_permlane16_swap_b32_e32 v23, v27
	v_add_f32_e32 v28, v23, v27
	v_add_f32_e32 v23, v30, v31
	s_waitcnt vmcnt(5)
	v_pk_fma_f32 v[30:31], v[14:15], v[48:49], v[36:37]
	v_pk_fma_f32 v[36:37], v[12:13], v[46:47], v[64:65]
	s_waitcnt vmcnt(4)
	v_pk_fma_f32 v[30:31], v[10:11], v[52:53], v[30:31]
	v_pk_fma_f32 v[36:37], v[8:9], v[50:51], v[36:37]
	v_add_f32_e32 v27, v62, v63
	v_add_f32_e32 v36, v36, v37
	v_add_f32_e32 v30, v30, v31
	v_add_f32_e32 v23, v23, v27
	v_add_f32_e32 v30, v36, v30
	v_add_f32_dpp v20, v20, v20 row_ror:4 row_mask:0xf bank_mask:0xf bound_ctrl:1
	v_add_f32_dpp v23, v23, v23 quad_perm:[1,0,3,2] row_mask:0xf bank_mask:0xf bound_ctrl:1
	v_add_f32_dpp v30, v30, v30 quad_perm:[1,0,3,2] row_mask:0xf bank_mask:0xf bound_ctrl:1
	v_add_f32_dpp v20, v20, v20 row_ror:8 row_mask:0xf bank_mask:0xf bound_ctrl:1
	v_add_f32_dpp v23, v23, v23 quad_perm:[2,3,0,1] row_mask:0xf bank_mask:0xf bound_ctrl:1
	v_add_f32_dpp v30, v30, v30 quad_perm:[2,3,0,1] row_mask:0xf bank_mask:0xf bound_ctrl:1
	v_mov_b32_e32 v21, v20
	v_add_f32_dpp v23, v23, v23 row_ror:4 row_mask:0xf bank_mask:0xf bound_ctrl:1
	v_add_f32_dpp v30, v30, v30 row_ror:4 row_mask:0xf bank_mask:0xf bound_ctrl:1
	v_permlane16_swap_b32_e32 v20, v21
	v_add_f32_dpp v23, v23, v23 row_ror:8 row_mask:0xf bank_mask:0xf bound_ctrl:1
	v_add_f32_dpp v30, v30, v30 row_ror:8 row_mask:0xf bank_mask:0xf bound_ctrl:1
	v_mov_b32_e32 v27, v23
	v_mov_b32_e32 v31, v30
	s_nop 0
	v_permlane16_swap_b32_e32 v23, v27
	v_permlane16_swap_b32_e32 v30, v31
	v_add_f32_e32 v21, v20, v21
	v_add_f32_e32 v23, v23, v27
	v_add_f32_e32 v30, v30, v31
	v_mov_b32_e32 v19, v16
	v_mov_b32_e32 v20, v17
	v_mov_b32_e32 v22, v18
	v_mov_b32_e32 v26, v21
	v_mov_b32_e32 v29, v28
	v_mov_b32_e32 v27, v23
	v_mov_b32_e32 v31, v30
	v_permlane32_swap_b32_e32 v16, v19
	v_permlane32_swap_b32_e32 v17, v20
	v_permlane32_swap_b32_e32 v18, v22
	v_permlane32_swap_b32_e32 v21, v26
	v_permlane32_swap_b32_e32 v28, v29
	v_permlane32_swap_b32_e32 v23, v27
	s_waitcnt vmcnt(2)
	v_pk_mul_f32 v[6:7], v[6:7], v[56:57]
	v_pk_mul_f32 v[4:5], v[4:5], v[54:55]
	v_pk_fma_f32 v[2:3], v[2:3], v[40:41], v[6:7]
	v_pk_fma_f32 v[0:1], v[0:1], v[38:39], v[4:5]
	v_permlane32_swap_b32_e32 v30, v31
	s_waitcnt vmcnt(1)
	v_pk_fma_f32 v[2:3], v[14:15], v[44:45], v[2:3]
	v_pk_fma_f32 v[0:1], v[12:13], v[42:43], v[0:1]
	s_waitcnt vmcnt(0)
	v_pk_fma_f32 v[2:3], v[10:11], v[34:35], v[2:3]
	v_pk_fma_f32 v[0:1], v[8:9], v[32:33], v[0:1]
	s_nop 0
	v_add_f32_e32 v0, v0, v1
	v_add_f32_e32 v1, v2, v3
	v_add_f32_e32 v0, v0, v1
	s_nop 1
	v_add_f32_dpp v0, v0, v0 quad_perm:[1,0,3,2] row_mask:0xf bank_mask:0xf bound_ctrl:1
	s_nop 1
	v_add_f32_dpp v0, v0, v0 quad_perm:[2,3,0,1] row_mask:0xf bank_mask:0xf bound_ctrl:1
	s_nop 1
	v_add_f32_dpp v0, v0, v0 row_ror:4 row_mask:0xf bank_mask:0xf bound_ctrl:1
	s_nop 1
	v_add_f32_dpp v0, v0, v0 row_ror:8 row_mask:0xf bank_mask:0xf bound_ctrl:1
	v_mov_b32_e32 v1, v0
	s_nop 1
	v_permlane16_swap_b32_e32 v0, v1
	v_add_f32_e32 v0, v0, v1
	v_mov_b32_e32 v1, v0
	s_nop 1
	v_permlane32_swap_b32_e32 v0, v1
	s_and_saveexec_b64 s[0:1], vcc
	s_cbranch_execz .LBB1_4
	v_add_f32_e32 v6, v16, v19
	v_cmp_eq_u32_e32 vcc, 0, v24
	v_add_f32_e32 v5, v17, v20
	v_add_f32_e32 v4, v18, v22
	v_cndmask_b32_e32 v6, 0, v6, vcc
	v_cmp_eq_u32_e32 vcc, 1, v24
	v_add_f32_e32 v3, v21, v26
	v_add_f32_e32 v2, v28, v29
	v_cndmask_b32_e32 v5, v6, v5, vcc
	v_cmp_eq_u32_e32 vcc, 2, v24
	v_add_f32_e32 v0, v0, v1
	v_add_f32_e32 v1, v30, v31
	v_cndmask_b32_e32 v4, v5, v4, vcc
	v_cmp_eq_u32_e32 vcc, 3, v24
	s_lshl_b32 s0, s8, 13
	s_and_b32 s0, s0, 0x1e000
	v_cndmask_b32_e32 v3, v4, v3, vcc
	v_cmp_eq_u32_e32 vcc, 4, v24
	s_add_u32 s0, s6, s0
	s_addc_u32 s1, s7, 0
	v_cndmask_b32_e32 v2, v3, v2, vcc
	v_add_f32_e32 v3, v23, v27
	v_cmp_eq_u32_e32 vcc, 5, v24
	s_nop 1
	v_cndmask_b32_e32 v2, v2, v3, vcc
	v_cmp_eq_u32_e32 vcc, 6, v24
	s_nop 1
	v_cndmask_b32_e32 v1, v2, v1, vcc
	v_cmp_eq_u32_e32 vcc, 7, v24
	s_nop 1
	v_cndmask_b32_e32 v2, v1, v0, vcc
	v_add_u32_e32 v0, s9, v25
	v_ashrrev_i32_e32 v0, 4, v0
	v_ashrrev_i32_e32 v1, 31, v0
	v_lshl_add_u64 v[0:1], v[0:1], 2, s[0:1]
	v_add_co_u32_e32 v0, vcc, 0x6000, v0
	s_nop 1
	v_addc_co_u32_e32 v1, vcc, 0, v1, vcc
	global_store_dword v[0:1], v2, off offset:64
